# v35 + G1 K-loop LDS-DMA pieces rebalanced 2/6/2/6 -> 4/4/4/4 per load segment (A half-0 staged one segment later, SP2 wait vmcnt(6))
# speedup vs baseline: 1.0137x; 1.0080x over previous
.LBB0_514:
	s_add_u32 s22, s82, s92
	s_addc_u32 s23, s83, s93
	s_add_u32 s24, s22, 0x100
	s_addc_u32 s25, s23, 0
	s_add_u32 s58, s3, s92
	s_addc_u32 s59, s2, s93
	s_add_i32 vcc_lo, 0, 0x10000
	s_cmpk_eq_i32 s92, 0xf00
	s_cselect_b64 s[26:27], -1, 0
	s_and_b64 s[22:23], s[26:27], exec
	s_cselect_b32 s25, s67, s25
	s_cselect_b32 s24, s75, s24
	s_cselect_b32 s23, s95, s59
	s_cselect_b32 s22, s29, s58
	s_add_u32 s58, s82, s92
	s_addc_u32 s59, s83, s93
	s_add_u32 s58, s58, s42
	s_addc_u32 s59, s59, s43
	s_add_i32 vcc_hi, 0, 0x14000
	v_add_u32_e32 v130, vcc_lo, v223
	v_add_u32_e32 v142, vcc_hi, v223
	ds_read_b128 v[146:149], v130
	ds_read_b128 v[150:153], v130 offset:1024
	ds_read_b128 v[154:157], v130 offset:2048
	ds_read_b128 v[158:161], v130 offset:3072
	ds_read_b128 v[130:133], v142
	ds_read_b128 v[134:137], v142 offset:1024
	ds_read_b128 v[138:141], v142 offset:2048
	ds_read_b128 v[142:145], v142 offset:3072
	v_lshl_add_u64 v[214:215], s[58:59], 0, v[198:199]
	s_mov_b32 m0, s91
	ds_read_b128 v[162:165], v224
	ds_read_b128 v[166:169], v224 offset:1024
	ds_read_b128 v[170:173], v224 offset:2048
	ds_read_b128 v[174:177], v224 offset:3072
	ds_read_b128 v[178:181], v224 offset:4096
	ds_read_b128 v[182:185], v224 offset:5120
	ds_read_b128 v[186:189], v224 offset:6144
	ds_read_b128 v[190:193], v224 offset:7168
	global_load_lds_dwordx4 v[214:215], off
	v_lshl_add_u64 v[214:215], s[58:59], 0, v[202:203]
	s_mov_b32 m0, s94
	s_nop 0
	global_load_lds_dwordx4 v[214:215], off
	v_lshl_add_u64 v[214:215], v[210:211], 0, s[92:93]
	s_add_i32 m0, s81, 0xc000
	s_nop 0
	global_load_lds_dwordx4 v[214:215], off
	v_lshl_add_u64 v[214:215], v[212:213], 0, s[92:93]
	s_add_i32 m0, s81, 0xe000
	s_nop 0
	global_load_lds_dwordx4 v[214:215], off
	s_waitcnt vmcnt(8)
	s_waitcnt lgkmcnt(0)
	s_barrier
	v_mfma_f32_16x16x32_bf16 v[124:127], v[146:149], v[162:165], v[124:127]
	v_mfma_f32_16x16x32_bf16 v[120:123], v[154:157], v[162:165], v[120:123]
	v_mfma_f32_16x16x32_bf16 v[116:119], v[146:149], v[170:173], v[116:119]
	v_mfma_f32_16x16x32_bf16 v[108:111], v[154:157], v[170:173], v[108:111]
	v_mfma_f32_16x16x32_bf16 v[100:103], v[146:149], v[178:181], v[100:103]
	v_mfma_f32_16x16x32_bf16 v[92:95], v[154:157], v[178:181], v[92:95]
	v_mfma_f32_16x16x32_bf16 v[84:87], v[146:149], v[186:189], v[84:87]
	v_mfma_f32_16x16x32_bf16 v[76:79], v[154:157], v[186:189], v[76:79]
	v_mfma_f32_16x16x32_bf16 v[124:127], v[150:153], v[166:169], v[124:127]
	v_mfma_f32_16x16x32_bf16 v[120:123], v[158:161], v[166:169], v[120:123]
	v_mfma_f32_16x16x32_bf16 v[116:119], v[150:153], v[174:177], v[116:119]
	v_mfma_f32_16x16x32_bf16 v[108:111], v[158:161], v[174:177], v[108:111]
	v_mfma_f32_16x16x32_bf16 v[100:103], v[150:153], v[182:185], v[100:103]
	v_mfma_f32_16x16x32_bf16 v[92:95], v[158:161], v[182:185], v[92:95]
	v_mfma_f32_16x16x32_bf16 v[84:87], v[150:153], v[190:193], v[84:87]
	v_mfma_f32_16x16x32_bf16 v[76:79], v[158:161], v[190:193], v[76:79]
	v_mfma_f32_16x16x32_bf16 v[112:115], v[130:133], v[162:165], v[112:115]
	v_mfma_f32_16x16x32_bf16 v[104:107], v[138:141], v[162:165], v[104:107]
	v_mfma_f32_16x16x32_bf16 v[96:99], v[130:133], v[170:173], v[96:99]
	v_mfma_f32_16x16x32_bf16 v[88:91], v[138:141], v[170:173], v[88:91]
	v_mfma_f32_16x16x32_bf16 v[80:83], v[130:133], v[178:181], v[80:83]
	v_mfma_f32_16x16x32_bf16 v[72:75], v[138:141], v[178:181], v[72:75]
	v_mfma_f32_16x16x32_bf16 v[68:71], v[130:133], v[186:189], v[68:71]
	v_mfma_f32_16x16x32_bf16 v[64:67], v[138:141], v[186:189], v[64:67]
	v_mfma_f32_16x16x32_bf16 v[112:115], v[134:137], v[166:169], v[112:115]
	v_mfma_f32_16x16x32_bf16 v[104:107], v[142:145], v[166:169], v[104:107]
	v_mfma_f32_16x16x32_bf16 v[96:99], v[134:137], v[174:177], v[96:99]
	v_mfma_f32_16x16x32_bf16 v[88:91], v[142:145], v[174:177], v[88:91]
	v_mfma_f32_16x16x32_bf16 v[80:83], v[134:137], v[182:185], v[80:83]
	v_mfma_f32_16x16x32_bf16 v[72:75], v[142:145], v[182:185], v[72:75]
	v_mfma_f32_16x16x32_bf16 v[68:71], v[134:137], v[190:193], v[68:71]
	v_mfma_f32_16x16x32_bf16 v[64:67], v[142:145], v[190:193], v[64:67]
	s_barrier
	s_add_i32 s58, vcc_lo, s28
	v_lshl_add_u64 v[214:215], s[22:23], 0, v[200:201]
	s_mov_b32 m0, s58
	ds_read_b128 v[186:189], v224 offset:16384
	ds_read_b128 v[190:193], v224 offset:17408
	ds_read_b128 v[178:181], v224 offset:18432
	ds_read_b128 v[182:185], v224 offset:19456
	ds_read_b128 v[170:173], v224 offset:20480
	ds_read_b128 v[174:177], v224 offset:21504
	ds_read_b128 v[162:165], v224 offset:22528
	ds_read_b128 v[166:169], v224 offset:23552
	global_load_lds_dwordx4 v[214:215], off
	s_add_i32 m0, s58, 0x2000
	s_add_u32 s58, s22, 0x80000
	v_lshl_add_u64 v[216:217], s[22:23], 0, v[204:205]
	s_addc_u32 s59, s23, 0
	s_add_i32 vcc_lo, vcc_hi, s28
	global_load_lds_dwordx4 v[216:217], off
	v_lshl_add_u64 v[218:219], s[58:59], 0, v[200:201]
	s_mov_b32 m0, vcc_lo
	global_load_lds_dwordx4 v[218:219], off
	v_lshl_add_u64 v[218:219], s[58:59], 0, v[204:205]
	s_add_i32 m0, vcc_lo, 0x2000
	v_cndmask_b32_e64 v194, 0, 1, s[96:97]
	global_load_lds_dwordx4 v[218:219], off
	v_cmp_ne_u32_e64 s[58:59], 1, v194
	s_andn2_b64 vcc, exec, s[96:97]
	s_waitcnt vmcnt(6)
	s_waitcnt lgkmcnt(0)
	s_barrier
	s_cbranch_vccnz .LBB0_516
	s_waitcnt lgkmcnt(0)
	v_mfma_f32_16x16x32_bf16 v[60:63], v[146:149], v[186:189], v[60:63]
	v_mfma_f32_16x16x32_bf16 v[56:59], v[154:157], v[186:189], v[56:59]
	v_mfma_f32_16x16x32_bf16 v[44:47], v[146:149], v[178:181], v[44:47]
	v_mfma_f32_16x16x32_bf16 v[40:43], v[154:157], v[178:181], v[40:43]
	v_mfma_f32_16x16x32_bf16 v[28:31], v[146:149], v[170:173], v[28:31]
	v_mfma_f32_16x16x32_bf16 v[24:27], v[154:157], v[170:173], v[24:27]
	v_mfma_f32_16x16x32_bf16 v[12:15], v[146:149], v[162:165], v[12:15]
	v_mfma_f32_16x16x32_bf16 v[8:11], v[154:157], v[162:165], v[8:11]
	v_mfma_f32_16x16x32_bf16 v[60:63], v[150:153], v[190:193], v[60:63]
	v_mfma_f32_16x16x32_bf16 v[56:59], v[158:161], v[190:193], v[56:59]
	v_mfma_f32_16x16x32_bf16 v[44:47], v[150:153], v[182:185], v[44:47]
	v_mfma_f32_16x16x32_bf16 v[40:43], v[158:161], v[182:185], v[40:43]
	v_mfma_f32_16x16x32_bf16 v[28:31], v[150:153], v[174:177], v[28:31]
	v_mfma_f32_16x16x32_bf16 v[24:27], v[158:161], v[174:177], v[24:27]
	v_mfma_f32_16x16x32_bf16 v[12:15], v[150:153], v[166:169], v[12:15]
	v_mfma_f32_16x16x32_bf16 v[8:11], v[158:161], v[166:169], v[8:11]
	v_mfma_f32_16x16x32_bf16 v[52:55], v[130:133], v[186:189], v[52:55]
	v_mfma_f32_16x16x32_bf16 v[48:51], v[138:141], v[186:189], v[48:51]
	v_mfma_f32_16x16x32_bf16 v[36:39], v[130:133], v[178:181], v[36:39]
	v_mfma_f32_16x16x32_bf16 v[32:35], v[138:141], v[178:181], v[32:35]
	v_mfma_f32_16x16x32_bf16 v[20:23], v[130:133], v[170:173], v[20:23]
	v_mfma_f32_16x16x32_bf16 v[16:19], v[138:141], v[170:173], v[16:19]
	v_mfma_f32_16x16x32_bf16 v[4:7], v[130:133], v[162:165], v[4:7]
	v_mfma_f32_16x16x32_bf16 v[0:3], v[138:141], v[162:165], v[0:3]
	v_mfma_f32_16x16x32_bf16 v[52:55], v[134:137], v[190:193], v[52:55]
	v_mfma_f32_16x16x32_bf16 v[48:51], v[142:145], v[190:193], v[48:51]
	v_mfma_f32_16x16x32_bf16 v[36:39], v[134:137], v[182:185], v[36:39]
	v_mfma_f32_16x16x32_bf16 v[32:35], v[142:145], v[182:185], v[32:35]
	v_mfma_f32_16x16x32_bf16 v[20:23], v[134:137], v[174:177], v[20:23]
	v_mfma_f32_16x16x32_bf16 v[16:19], v[142:145], v[174:177], v[16:19]
	v_mfma_f32_16x16x32_bf16 v[4:7], v[134:137], v[166:169], v[4:7]
	v_mfma_f32_16x16x32_bf16 v[0:3], v[142:145], v[166:169], v[0:3]
.LBB0_516:
	s_barrier
	s_add_i32 vcc_lo, 0, 0x18000
	s_add_i32 vcc_hi, 0, 0x1c000
	v_add_u32_e32 v130, vcc_lo, v223
	v_add_u32_e32 v142, vcc_hi, v223
	ds_read_b128 v[146:149], v130
	ds_read_b128 v[150:153], v130 offset:1024
	ds_read_b128 v[154:157], v130 offset:2048
	ds_read_b128 v[158:161], v130 offset:3072
	ds_read_b128 v[130:133], v142
	ds_read_b128 v[134:137], v142 offset:1024
	ds_read_b128 v[138:141], v142 offset:2048
	ds_read_b128 v[142:145], v142 offset:3072
	v_lshl_add_u64 v[218:219], s[24:25], 0, v[198:199]
	v_lshl_add_u64 v[220:221], s[24:25], 0, v[202:203]
	s_and_b64 s[26:27], s[26:27], exec
	s_cselect_b32 s27, s72, s86
	s_cselect_b32 s26, 0, s87
	s_add_u32 s24, s24, s27
	s_addc_u32 s25, s25, s26
	v_lshl_add_u64 v[226:227], s[24:25], 0, v[198:199]
	ds_read_b128 v[162:165], v224 offset:32768
	ds_read_b128 v[166:169], v224 offset:33792
	ds_read_b128 v[170:173], v224 offset:34816
	ds_read_b128 v[174:177], v224 offset:35840
	ds_read_b128 v[178:181], v224 offset:36864
	ds_read_b128 v[182:185], v224 offset:37888
	ds_read_b128 v[186:189], v224 offset:38912
	ds_read_b128 v[190:193], v224 offset:39936
	s_mov_b32 m0, s81
	s_nop 0
	global_load_lds_dwordx4 v[218:219], off
	s_mov_b32 m0, s88
	s_nop 0
	global_load_lds_dwordx4 v[220:221], off
	s_mov_b32 m0, s89
	s_nop 0
	global_load_lds_dwordx4 v[226:227], off
	v_lshl_add_u64 v[226:227], s[24:25], 0, v[202:203]
	s_mov_b32 m0, s90
	s_nop 0
	global_load_lds_dwordx4 v[226:227], off
	s_waitcnt vmcnt(8)
	s_waitcnt lgkmcnt(0)
	s_barrier
	v_mfma_f32_16x16x32_bf16 v[124:127], v[146:149], v[162:165], v[124:127]
	v_mfma_f32_16x16x32_bf16 v[120:123], v[154:157], v[162:165], v[120:123]
	v_mfma_f32_16x16x32_bf16 v[116:119], v[146:149], v[170:173], v[116:119]
	v_mfma_f32_16x16x32_bf16 v[108:111], v[154:157], v[170:173], v[108:111]
	v_mfma_f32_16x16x32_bf16 v[100:103], v[146:149], v[178:181], v[100:103]
	v_mfma_f32_16x16x32_bf16 v[92:95], v[154:157], v[178:181], v[92:95]
	v_mfma_f32_16x16x32_bf16 v[84:87], v[146:149], v[186:189], v[84:87]
	v_mfma_f32_16x16x32_bf16 v[76:79], v[154:157], v[186:189], v[76:79]
	v_mfma_f32_16x16x32_bf16 v[124:127], v[150:153], v[166:169], v[124:127]
	v_mfma_f32_16x16x32_bf16 v[120:123], v[158:161], v[166:169], v[120:123]
	v_mfma_f32_16x16x32_bf16 v[116:119], v[150:153], v[174:177], v[116:119]
	v_mfma_f32_16x16x32_bf16 v[108:111], v[158:161], v[174:177], v[108:111]
	v_mfma_f32_16x16x32_bf16 v[100:103], v[150:153], v[182:185], v[100:103]
	v_mfma_f32_16x16x32_bf16 v[92:95], v[158:161], v[182:185], v[92:95]
	v_mfma_f32_16x16x32_bf16 v[84:87], v[150:153], v[190:193], v[84:87]
	v_mfma_f32_16x16x32_bf16 v[76:79], v[158:161], v[190:193], v[76:79]
	v_mfma_f32_16x16x32_bf16 v[112:115], v[130:133], v[162:165], v[112:115]
	v_mfma_f32_16x16x32_bf16 v[104:107], v[138:141], v[162:165], v[104:107]
	v_mfma_f32_16x16x32_bf16 v[96:99], v[130:133], v[170:173], v[96:99]
	v_mfma_f32_16x16x32_bf16 v[88:91], v[138:141], v[170:173], v[88:91]
	v_mfma_f32_16x16x32_bf16 v[80:83], v[130:133], v[178:181], v[80:83]
	v_mfma_f32_16x16x32_bf16 v[72:75], v[138:141], v[178:181], v[72:75]
	v_mfma_f32_16x16x32_bf16 v[68:71], v[130:133], v[186:189], v[68:71]
	v_mfma_f32_16x16x32_bf16 v[64:67], v[138:141], v[186:189], v[64:67]
	v_mfma_f32_16x16x32_bf16 v[112:115], v[134:137], v[166:169], v[112:115]
	v_mfma_f32_16x16x32_bf16 v[104:107], v[142:145], v[166:169], v[104:107]
	v_mfma_f32_16x16x32_bf16 v[96:99], v[134:137], v[174:177], v[96:99]
	v_mfma_f32_16x16x32_bf16 v[88:91], v[142:145], v[174:177], v[88:91]
	v_mfma_f32_16x16x32_bf16 v[80:83], v[134:137], v[182:185], v[80:83]
	v_mfma_f32_16x16x32_bf16 v[72:75], v[142:145], v[182:185], v[72:75]
	v_mfma_f32_16x16x32_bf16 v[68:71], v[134:137], v[190:193], v[68:71]
	v_mfma_f32_16x16x32_bf16 v[64:67], v[142:145], v[190:193], v[64:67]
	s_barrier
	s_add_i32 s24, vcc_lo, s28
	v_lshl_add_u64 v[214:215], v[214:215], 0, s[42:43]
	s_mov_b32 m0, s24
	ds_read_b128 v[186:189], v224 offset:49152
	ds_read_b128 v[190:193], v224 offset:50176
	ds_read_b128 v[178:181], v224 offset:51200
	ds_read_b128 v[182:185], v224 offset:52224
	ds_read_b128 v[170:173], v224 offset:53248
	ds_read_b128 v[174:177], v224 offset:54272
	ds_read_b128 v[162:165], v224 offset:55296
	ds_read_b128 v[166:169], v224 offset:56320
	global_load_lds_dwordx4 v[214:215], off
	s_add_i32 m0, s24, 0x2000
	s_add_u32 s22, s22, 0x80080
	v_lshl_add_u64 v[214:215], v[216:217], 0, s[42:43]
	s_addc_u32 s23, s23, 0
	s_add_i32 s24, vcc_hi, s28
	global_load_lds_dwordx4 v[214:215], off
	v_lshl_add_u64 v[214:215], s[22:23], 0, v[200:201]
	s_mov_b32 m0, s24
	s_and_b64 vcc, exec, s[58:59]
	global_load_lds_dwordx4 v[214:215], off
	v_lshl_add_u64 v[214:215], s[22:23], 0, v[204:205]
	s_add_i32 m0, s24, 0x2000
	s_nop 0
	global_load_lds_dwordx4 v[214:215], off
	s_waitcnt vmcnt(6)
	s_waitcnt lgkmcnt(0)
	s_barrier
	s_cbranch_vccnz .LBB0_513
	s_waitcnt lgkmcnt(0)
	v_mfma_f32_16x16x32_bf16 v[60:63], v[146:149], v[186:189], v[60:63]
	v_mfma_f32_16x16x32_bf16 v[56:59], v[154:157], v[186:189], v[56:59]
	v_mfma_f32_16x16x32_bf16 v[44:47], v[146:149], v[178:181], v[44:47]
	v_mfma_f32_16x16x32_bf16 v[40:43], v[154:157], v[178:181], v[40:43]
	v_mfma_f32_16x16x32_bf16 v[28:31], v[146:149], v[170:173], v[28:31]
	v_mfma_f32_16x16x32_bf16 v[24:27], v[154:157], v[170:173], v[24:27]
	v_mfma_f32_16x16x32_bf16 v[12:15], v[146:149], v[162:165], v[12:15]
	v_mfma_f32_16x16x32_bf16 v[8:11], v[154:157], v[162:165], v[8:11]
	v_mfma_f32_16x16x32_bf16 v[60:63], v[150:153], v[190:193], v[60:63]
	v_mfma_f32_16x16x32_bf16 v[56:59], v[158:161], v[190:193], v[56:59]
	v_mfma_f32_16x16x32_bf16 v[44:47], v[150:153], v[182:185], v[44:47]
	v_mfma_f32_16x16x32_bf16 v[40:43], v[158:161], v[182:185], v[40:43]
	v_mfma_f32_16x16x32_bf16 v[28:31], v[150:153], v[174:177], v[28:31]
	v_mfma_f32_16x16x32_bf16 v[24:27], v[158:161], v[174:177], v[24:27]
	v_mfma_f32_16x16x32_bf16 v[12:15], v[150:153], v[166:169], v[12:15]
	v_mfma_f32_16x16x32_bf16 v[8:11], v[158:161], v[166:169], v[8:11]
	v_mfma_f32_16x16x32_bf16 v[52:55], v[130:133], v[186:189], v[52:55]
	v_mfma_f32_16x16x32_bf16 v[48:51], v[138:141], v[186:189], v[48:51]
	v_mfma_f32_16x16x32_bf16 v[36:39], v[130:133], v[178:181], v[36:39]
	v_mfma_f32_16x16x32_bf16 v[32:35], v[138:141], v[178:181], v[32:35]
	v_mfma_f32_16x16x32_bf16 v[20:23], v[130:133], v[170:173], v[20:23]
	v_mfma_f32_16x16x32_bf16 v[16:19], v[138:141], v[170:173], v[16:19]
	v_mfma_f32_16x16x32_bf16 v[4:7], v[130:133], v[162:165], v[4:7]
	v_mfma_f32_16x16x32_bf16 v[0:3], v[138:141], v[162:165], v[0:3]
	v_mfma_f32_16x16x32_bf16 v[52:55], v[134:137], v[190:193], v[52:55]
	v_mfma_f32_16x16x32_bf16 v[48:51], v[142:145], v[190:193], v[48:51]
	v_mfma_f32_16x16x32_bf16 v[36:39], v[134:137], v[182:185], v[36:39]
	v_mfma_f32_16x16x32_bf16 v[32:35], v[142:145], v[182:185], v[32:35]
	v_mfma_f32_16x16x32_bf16 v[20:23], v[134:137], v[174:177], v[20:23]
	v_mfma_f32_16x16x32_bf16 v[16:19], v[142:145], v[174:177], v[16:19]
	v_mfma_f32_16x16x32_bf16 v[4:7], v[134:137], v[166:169], v[4:7]
	v_mfma_f32_16x16x32_bf16 v[0:3], v[142:145], v[166:169], v[0:3]
	s_branch .LBB0_513
